# attention: cross-half row max through v_permlane32_swap instead of ds_bpermute (on top of skip-zero-rescale, prefetch, finalize, no-copy)
# speedup vs baseline: 1.0053x; 1.0053x over previous
.LBB0_730:
	s_nop 6
	v_max_f32_e32 v66, v131, v131
	v_max_f32_e32 v67, v130, v130
	v_max_f32_e32 v66, v67, v66
	v_max3_f32 v66, v66, v132, v133
	v_max3_f32 v66, v66, v134, v135
	v_max3_f32 v66, v66, v136, v137
	v_max3_f32 v66, v66, v138, v139
	v_max3_f32 v66, v66, v140, v141
	v_max3_f32 v66, v66, v142, v143
	v_max3_f32 v66, v66, v144, v145
	s_waitcnt lgkmcnt(4)
	v_add3_u32 v70, v69, v185, v194
	ds_read_b64_tr_b16 v[114:115], v70 offset:8192
	v_add3_u32 v71, v69, v187, v195
	ds_read_b64_tr_b16 v[116:117], v71 offset:8192
	v_add3_u32 v70, v69, v185, v197
	ds_read_b64_tr_b16 v[118:119], v70 offset:8192
	v_add3_u32 v71, v69, v187, v198
	ds_read_b64_tr_b16 v[120:121], v71 offset:8192
	v_add3_u32 v70, v69, v184, v194
	ds_read_b64_tr_b16 v[122:123], v70 offset:8192
	v_add3_u32 v71, v69, v189, v196
	ds_read_b64_tr_b16 v[124:125], v71 offset:8192
	v_add3_u32 v70, v69, v184, v197
	ds_read_b64_tr_b16 v[126:127], v70 offset:8192
	v_add3_u32 v71, v69, v189, v199
	ds_read_b64_tr_b16 v[128:129], v71 offset:8192
	v_mov_b32_e32 v67, v66
	s_nop 1
	v_permlane32_swap_b32_e32 v67, v66
	v_max_f32_e32 v66, v66, v67
	v_add_f32_e32 v67, 0x40c00000, v231
	v_cmp_gt_f32_e32 vcc, v66, v67
	s_nop 1
	v_cndmask_b32_e32 v233, v231, v66, vcc
	v_sub_f32_e32 v66, v231, v233
	v_exp_f32_e32 v146, v66
	s_cbranch_vccz .LBB0_732
	v_cmp_ne_u32_e32 vcc, 0xf149f2ca, v231
	s_cbranch_vccz .LBB0_732
	v_pk_mul_f32 v[64:65], v[64:65], v[146:147] op_sel_hi:[1,0]
	v_pk_mul_f32 v[62:63], v[62:63], v[146:147] op_sel_hi:[1,0]
	v_pk_mul_f32 v[60:61], v[60:61], v[146:147] op_sel_hi:[1,0]
	v_pk_mul_f32 v[58:59], v[58:59], v[146:147] op_sel_hi:[1,0]
	v_pk_mul_f32 v[56:57], v[56:57], v[146:147] op_sel_hi:[1,0]
	v_pk_mul_f32 v[54:55], v[54:55], v[146:147] op_sel_hi:[1,0]
	v_pk_mul_f32 v[52:53], v[52:53], v[146:147] op_sel_hi:[1,0]
	v_pk_mul_f32 v[50:51], v[50:51], v[146:147] op_sel_hi:[1,0]
	v_pk_mul_f32 v[48:49], v[48:49], v[146:147] op_sel_hi:[1,0]
	v_pk_mul_f32 v[46:47], v[46:47], v[146:147] op_sel_hi:[1,0]
	v_pk_mul_f32 v[44:45], v[44:45], v[146:147] op_sel_hi:[1,0]
	v_pk_mul_f32 v[42:43], v[42:43], v[146:147] op_sel_hi:[1,0]
	v_pk_mul_f32 v[40:41], v[40:41], v[146:147] op_sel_hi:[1,0]
	v_pk_mul_f32 v[38:39], v[38:39], v[146:147] op_sel_hi:[1,0]
	v_pk_mul_f32 v[36:37], v[36:37], v[146:147] op_sel_hi:[1,0]
	v_pk_mul_f32 v[34:35], v[34:35], v[146:147] op_sel_hi:[1,0]
	v_pk_mul_f32 v[32:33], v[32:33], v[146:147] op_sel_hi:[1,0]
	v_pk_mul_f32 v[30:31], v[30:31], v[146:147] op_sel_hi:[1,0]
	v_pk_mul_f32 v[28:29], v[28:29], v[146:147] op_sel_hi:[1,0]
	v_pk_mul_f32 v[26:27], v[26:27], v[146:147] op_sel_hi:[1,0]
	v_pk_mul_f32 v[24:25], v[24:25], v[146:147] op_sel_hi:[1,0]
	v_pk_mul_f32 v[22:23], v[22:23], v[146:147] op_sel_hi:[1,0]
	v_pk_mul_f32 v[20:21], v[20:21], v[146:147] op_sel_hi:[1,0]
	v_pk_mul_f32 v[18:19], v[18:19], v[146:147] op_sel_hi:[1,0]
	v_pk_mul_f32 v[16:17], v[16:17], v[146:147] op_sel_hi:[1,0]
	v_pk_mul_f32 v[14:15], v[14:15], v[146:147] op_sel_hi:[1,0]
	v_pk_mul_f32 v[12:13], v[12:13], v[146:147] op_sel_hi:[1,0]
	v_pk_mul_f32 v[10:11], v[10:11], v[146:147] op_sel_hi:[1,0]
	v_pk_mul_f32 v[8:9], v[8:9], v[146:147] op_sel_hi:[1,0]
	v_pk_mul_f32 v[6:7], v[6:7], v[146:147] op_sel_hi:[1,0]
	v_pk_mul_f32 v[4:5], v[4:5], v[146:147] op_sel_hi:[1,0]
	v_pk_mul_f32 v[2:3], v[2:3], v[146:147] op_sel_hi:[1,0]
	s_branch .LBB0_733

.LBB0_800:
	s_nop 6
	v_max_f32_e32 v66, v131, v131
	v_max_f32_e32 v67, v130, v130
	v_max_f32_e32 v66, v67, v66
	v_max3_f32 v66, v66, v132, v133
	v_max3_f32 v66, v66, v134, v135
	v_max3_f32 v66, v66, v136, v137
	v_max3_f32 v66, v66, v138, v139
	v_max3_f32 v66, v66, v140, v141
	v_max3_f32 v66, v66, v142, v143
	v_max3_f32 v66, v66, v144, v145
	s_waitcnt lgkmcnt(4)
	v_add3_u32 v70, v69, v185, v194
	ds_read_b64_tr_b16 v[114:115], v70 offset:8192
	v_add3_u32 v71, v69, v187, v195
	ds_read_b64_tr_b16 v[116:117], v71 offset:8192
	v_add3_u32 v70, v69, v185, v197
	ds_read_b64_tr_b16 v[118:119], v70 offset:8192
	v_add3_u32 v71, v69, v187, v198
	ds_read_b64_tr_b16 v[120:121], v71 offset:8192
	v_add3_u32 v70, v69, v184, v194
	ds_read_b64_tr_b16 v[122:123], v70 offset:8192
	v_add3_u32 v71, v69, v189, v196
	ds_read_b64_tr_b16 v[124:125], v71 offset:8192
	v_add3_u32 v70, v69, v184, v197
	ds_read_b64_tr_b16 v[126:127], v70 offset:8192
	v_add3_u32 v71, v69, v189, v199
	ds_read_b64_tr_b16 v[128:129], v71 offset:8192
	v_mov_b32_e32 v67, v66
	s_nop 1
	v_permlane32_swap_b32_e32 v67, v66
	v_max_f32_e32 v66, v66, v67
	v_add_f32_e32 v67, 0x40c00000, v233
	v_cmp_gt_f32_e32 vcc, v66, v67
	s_nop 1
	v_cndmask_b32_e32 v235, v233, v66, vcc
	v_sub_f32_e32 v66, v233, v235
	v_exp_f32_e32 v146, v66
	s_cbranch_vccz .LBB0_802
	v_cmp_ne_u32_e32 vcc, 0xf149f2ca, v233
	s_cbranch_vccz .LBB0_802
	v_pk_mul_f32 v[64:65], v[64:65], v[146:147] op_sel_hi:[1,0]
	v_pk_mul_f32 v[62:63], v[62:63], v[146:147] op_sel_hi:[1,0]
	v_pk_mul_f32 v[60:61], v[60:61], v[146:147] op_sel_hi:[1,0]
	v_pk_mul_f32 v[58:59], v[58:59], v[146:147] op_sel_hi:[1,0]
	v_pk_mul_f32 v[56:57], v[56:57], v[146:147] op_sel_hi:[1,0]
	v_pk_mul_f32 v[54:55], v[54:55], v[146:147] op_sel_hi:[1,0]
	v_pk_mul_f32 v[52:53], v[52:53], v[146:147] op_sel_hi:[1,0]
	v_pk_mul_f32 v[50:51], v[50:51], v[146:147] op_sel_hi:[1,0]
	v_pk_mul_f32 v[48:49], v[48:49], v[146:147] op_sel_hi:[1,0]
	v_pk_mul_f32 v[46:47], v[46:47], v[146:147] op_sel_hi:[1,0]
	v_pk_mul_f32 v[44:45], v[44:45], v[146:147] op_sel_hi:[1,0]
	v_pk_mul_f32 v[42:43], v[42:43], v[146:147] op_sel_hi:[1,0]
	v_pk_mul_f32 v[40:41], v[40:41], v[146:147] op_sel_hi:[1,0]
	v_pk_mul_f32 v[38:39], v[38:39], v[146:147] op_sel_hi:[1,0]
	v_pk_mul_f32 v[36:37], v[36:37], v[146:147] op_sel_hi:[1,0]
	v_pk_mul_f32 v[34:35], v[34:35], v[146:147] op_sel_hi:[1,0]
	v_pk_mul_f32 v[32:33], v[32:33], v[146:147] op_sel_hi:[1,0]
	v_pk_mul_f32 v[30:31], v[30:31], v[146:147] op_sel_hi:[1,0]
	v_pk_mul_f32 v[28:29], v[28:29], v[146:147] op_sel_hi:[1,0]
	v_pk_mul_f32 v[26:27], v[26:27], v[146:147] op_sel_hi:[1,0]
	v_pk_mul_f32 v[24:25], v[24:25], v[146:147] op_sel_hi:[1,0]
	v_pk_mul_f32 v[22:23], v[22:23], v[146:147] op_sel_hi:[1,0]
	v_pk_mul_f32 v[20:21], v[20:21], v[146:147] op_sel_hi:[1,0]
	v_pk_mul_f32 v[18:19], v[18:19], v[146:147] op_sel_hi:[1,0]
	v_pk_mul_f32 v[16:17], v[16:17], v[146:147] op_sel_hi:[1,0]
	v_pk_mul_f32 v[14:15], v[14:15], v[146:147] op_sel_hi:[1,0]
	v_pk_mul_f32 v[12:13], v[12:13], v[146:147] op_sel_hi:[1,0]
	v_pk_mul_f32 v[10:11], v[10:11], v[146:147] op_sel_hi:[1,0]
	v_pk_mul_f32 v[8:9], v[8:9], v[146:147] op_sel_hi:[1,0]
	v_pk_mul_f32 v[6:7], v[6:7], v[146:147] op_sel_hi:[1,0]
	v_pk_mul_f32 v[4:5], v[4:5], v[146:147] op_sel_hi:[1,0]
	v_pk_mul_f32 v[2:3], v[2:3], v[146:147] op_sel_hi:[1,0]
	s_branch .LBB0_803
